# stack3_prio2
# baseline (speedup 1.0000x reference)
_Z6k_rec2PKiS0_S0_PK15HIP_vector_typeIjLj4EEPKfS6_PS2_PS1_IjLj2EEPf:
	v_readfirstlane_b32 s90, v0
	s_lshr_b32 s90, s90, 8
	s_load_dwordx2 s[6:7], s[0:1], 0x0
	s_load_dwordx2 s[4:5], s[0:1], 0x28
	v_cmp_gt_u32_e32 vcc, 32, v0
	s_and_saveexec_b64 s[8:9], vcc
	v_mov_b32_e32 v1, 0x22000
	v_lshl_or_b32 v1, v0, 2, v1
	v_mov_b32_e32 v2, 0
	ds_write_b32 v1, v2
	s_or_b64 exec, exec, s[8:9]
	v_mov_b32_e32 v3, 0
	v_lshlrev_b32_e32 v2, 2, v0
	s_waitcnt lgkmcnt(0)
	v_lshl_add_u64 v[4:5], s[6:7], 0, v[2:3]
	s_movk_i32 s3, 0x1000
	v_or_b32_e32 v1, 0x400, v0
	v_add_co_u32_e32 v6, vcc, s3, v4
	v_lshlrev_b32_e32 v3, 2, v1
	s_nop 0
	v_addc_co_u32_e32 v7, vcc, 0, v5, vcc
	global_load_dword v68, v2, s[6:7]
	global_load_dword v69, v2, s[6:7] offset:2048
	global_load_dword v70, v3, s[6:7]
	global_load_dword v71, v[6:7], off offset:2048
	v_or_b32_e32 v165, 0x800, v0
	s_movk_i32 s3, 0x2000
	v_lshlrev_b32_e32 v6, 2, v165
	v_add_co_u32_e32 v2, vcc, s3, v4
	v_or_b32_e32 v232, 0xc00, v0
	s_nop 0
	v_addc_co_u32_e32 v3, vcc, 0, v5, vcc
	global_load_dword v72, v6, s[6:7]
	global_load_dword v73, v[2:3], off offset:2048
	v_lshlrev_b32_e32 v2, 2, v232
	global_load_dword v74, v2, s[6:7]
	s_movk_i32 s3, 0x3000
	v_add_co_u32_e32 v2, vcc, s3, v4
	s_ashr_i32 s3, s2, 31
	s_nop 0
	v_addc_co_u32_e32 v3, vcc, 0, v5, vcc
	global_load_dword v75, v[2:3], off offset:2048
	s_lshl_b64 s[6:7], s[2:3], 17
	s_add_u32 s4, s4, s6
	s_addc_u32 s5, s5, s7
	v_mbcnt_lo_u32_b32 v77, -1, 0
	v_mbcnt_hi_u32_b32 v77, -1, v77
	v_and_b32_e32 v83, 64, v77
	v_xor_b32_e32 v84, 32, v77
	v_add_u32_e32 v83, 64, v83
	v_cmp_lt_i32_e32 vcc, v84, v83
	v_xor_b32_e32 v85, 16, v77
	v_xor_b32_e32 v86, 8, v77
	v_cndmask_b32_e32 v84, v77, v84, vcc
	v_lshlrev_b32_e32 v234, 2, v84
	v_cmp_lt_i32_e32 vcc, v85, v83
	v_xor_b32_e32 v87, 4, v77
	v_xor_b32_e32 v88, 2, v77
	v_cndmask_b32_e32 v85, v77, v85, vcc
	v_lshlrev_b32_e32 v235, 2, v85
	v_cmp_lt_i32_e32 vcc, v86, v83
	v_xor_b32_e32 v89, 1, v77
	v_mov_b32_e32 v76, 0x20000
	v_cndmask_b32_e32 v86, v77, v86, vcc
	v_lshlrev_b32_e32 v236, 2, v86
	v_cmp_lt_i32_e32 vcc, v87, v83
	v_lshl_or_b32 v79, v1, 1, v76
	v_lshl_or_b32 v81, v165, 1, v76
	v_cndmask_b32_e32 v87, v77, v87, vcc
	v_cmp_lt_i32_e32 vcc, v88, v83
	v_lshlrev_b32_e32 v237, 2, v87
	v_lshl_or_b32 v76, v232, 1, v76
	v_cndmask_b32_e32 v88, v77, v88, vcc
	v_cmp_lt_i32_e32 vcc, v89, v83
	v_lshlrev_b32_e32 v238, 2, v88
	s_mov_b32 s3, 0
	v_cndmask_b32_e32 v77, v77, v89, vcc
	v_lshlrev_b32_e32 v239, 2, v77
	s_waitcnt vmcnt(7)
	v_lshlrev_b32_e32 v2, 1, v68
	s_waitcnt vmcnt(6)
	v_lshlrev_b32_e32 v4, 1, v69
	v_ashrrev_i32_e32 v3, 31, v2
	v_ashrrev_i32_e32 v5, 31, v4
	v_lshl_add_u64 v[10:11], v[2:3], 4, s[4:5]
	v_lshl_add_u64 v[20:21], v[4:5], 4, s[4:5]
	global_load_dwordx4 v[2:5], v[10:11], off offset:16
	global_load_dwordx4 v[6:9], v[10:11], off
	s_nop 0
	global_load_dwordx4 v[10:13], v[20:21], off offset:16
	global_load_dwordx4 v[14:17], v[20:21], off
	s_waitcnt vmcnt(9)
	v_lshlrev_b32_e32 v18, 1, v70
	v_ashrrev_i32_e32 v19, 31, v18
	v_lshl_add_u64 v[28:29], v[18:19], 4, s[4:5]
	global_load_dwordx4 v[18:21], v[28:29], off offset:16
	global_load_dwordx4 v[22:25], v[28:29], off
	s_waitcnt vmcnt(10)
	v_lshlrev_b32_e32 v26, 1, v71
	v_ashrrev_i32_e32 v27, 31, v26
	v_lshl_add_u64 v[36:37], v[26:27], 4, s[4:5]
	global_load_dwordx4 v[26:29], v[36:37], off offset:16
	global_load_dwordx4 v[30:33], v[36:37], off
	s_waitcnt vmcnt(11)
	v_lshlrev_b32_e32 v34, 1, v72
	v_ashrrev_i32_e32 v35, 31, v34
	v_lshl_add_u64 v[44:45], v[34:35], 4, s[4:5]
	global_load_dwordx4 v[34:37], v[44:45], off offset:16
	global_load_dwordx4 v[38:41], v[44:45], off
	s_waitcnt vmcnt(12)
	v_lshlrev_b32_e32 v42, 1, v73
	v_ashrrev_i32_e32 v43, 31, v42
	v_lshl_add_u64 v[52:53], v[42:43], 4, s[4:5]
	global_load_dwordx4 v[42:45], v[52:53], off offset:16
	global_load_dwordx4 v[46:49], v[52:53], off
	s_waitcnt vmcnt(13)
	v_lshlrev_b32_e32 v50, 1, v74
	v_ashrrev_i32_e32 v51, 31, v50
	v_lshl_add_u64 v[58:59], v[50:51], 4, s[4:5]
	global_load_dwordx4 v[50:53], v[58:59], off offset:16
	global_load_dwordx4 v[54:57], v[58:59], off
	s_waitcnt vmcnt(14)
	v_lshlrev_b32_e32 v58, 1, v75
	v_ashrrev_i32_e32 v59, 31, v58
	v_lshl_add_u64 v[66:67], v[58:59], 4, s[4:5]
	global_load_dwordx4 v[62:65], v[66:67], off
	global_load_dwordx4 v[58:61], v[66:67], off offset:16
	v_lshlrev_b32_e32 v67, 1, v0
	v_or_b32_e32 v233, 0x20000, v67
	s_load_dwordx4 s[8:11], s[0:1], 0x8
	s_load_dwordx2 s[14:15], s[0:1], 0x18
	s_load_dwordx2 s[12:13], s[0:1], 0x40
	s_load_dwordx2 s[6:7], s[0:1], 0x30
	v_or_b32_e32 v78, 0x20400, v67
	v_or_b32_e32 v80, 0x20c00, v67
	ds_write_b16 v233, v68
	ds_write_b16 v78, v69
	ds_write_b16 v79, v70
	ds_write_b16 v80, v71
	v_or_b32_e32 v82, 0x21400, v67
	v_or_b32_e32 v67, 0x21c00, v67
	ds_write_b16 v81, v72
	ds_write_b16 v82, v73
	ds_write_b16 v76, v74
	ds_write_b16 v67, v75
	v_and_b32_e32 v66, 63, v0
	v_cmp_eq_u32_e64 s[4:5], 0, v66
	s_waitcnt lgkmcnt(0)
	s_barrier
	s_waitcnt vmcnt(14)
	v_max3_f32 v84, |v6|, 0, |v7|
	v_max3_f32 v84, v84, |v8|, |v9|
	v_max3_f32 v84, v84, |v2|, |v3|
	v_max3_f32 v84, v84, |v4|, |v5|
	s_waitcnt vmcnt(12)
	v_max3_f32 v84, v84, |v14|, |v15|
	v_max3_f32 v84, v84, |v16|, |v17|
	v_max3_f32 v84, v84, |v10|, |v11|
	v_max3_f32 v84, v84, |v12|, |v13|
	s_waitcnt vmcnt(10)
	v_max3_f32 v84, v84, |v22|, |v23|
	v_max3_f32 v84, v84, |v24|, |v25|
	v_max3_f32 v84, v84, |v18|, |v19|
	v_max3_f32 v84, v84, |v20|, |v21|
	s_waitcnt vmcnt(8)
	v_max3_f32 v84, v84, |v30|, |v31|
	v_max3_f32 v84, v84, |v32|, |v33|
	v_max3_f32 v84, v84, |v26|, |v27|
	v_max3_f32 v84, v84, |v28|, |v29|
	s_waitcnt vmcnt(6)
	v_max3_f32 v84, v84, |v38|, |v39|
	v_max3_f32 v84, v84, |v40|, |v41|
	v_max3_f32 v84, v84, |v34|, |v35|
	v_max3_f32 v84, v84, |v36|, |v37|
	s_waitcnt vmcnt(4)
	v_max3_f32 v84, v84, |v46|, |v47|
	v_max3_f32 v84, v84, |v48|, |v49|
	v_max3_f32 v84, v84, |v42|, |v43|
	v_max3_f32 v84, v84, |v44|, |v45|
	s_waitcnt vmcnt(2)
	v_max3_f32 v84, v84, |v54|, |v55|
	v_max3_f32 v84, v84, |v56|, |v57|
	v_max3_f32 v84, v84, |v50|, |v51|
	v_max3_f32 v84, v84, |v52|, |v53|
	s_waitcnt vmcnt(1)
	v_max3_f32 v84, v84, |v62|, |v63|
	v_max3_f32 v84, v84, |v64|, |v65|
	s_waitcnt vmcnt(0)
	v_max3_f32 v84, v84, |v58|, |v59|
	v_max3_f32 v84, v84, |v60|, |v61|
	ds_bpermute_b32 v90, v234, v84
	s_waitcnt lgkmcnt(0)
	v_max_f32_e32 v85, v90, v90
	v_max_f32_e32 v84, v84, v85
	ds_bpermute_b32 v85, v235, v84
	s_waitcnt lgkmcnt(0)
	v_max_f32_e32 v85, v85, v85
	v_max_f32_e32 v84, v84, v85
	ds_bpermute_b32 v85, v236, v84
	s_waitcnt lgkmcnt(0)
	v_max_f32_e32 v83, v85, v85
	v_max_f32_e32 v83, v84, v83
	ds_bpermute_b32 v84, v237, v83
	s_waitcnt lgkmcnt(0)
	v_max_f32_e32 v68, v84, v84
	v_max_f32_e32 v68, v83, v68
	ds_bpermute_b32 v69, v238, v68
	s_waitcnt lgkmcnt(0)
	v_max_f32_e32 v67, v69, v69
	v_max_f32_e32 v67, v68, v67
	ds_bpermute_b32 v68, v239, v67
	s_and_saveexec_b64 s[16:17], s[4:5]
	s_cbranch_execz .LBB3_7
	s_waitcnt lgkmcnt(0)
	v_max_f32_e32 v68, v68, v68
	v_max_f32_e32 v67, v67, v67
	s_mov_b64 s[18:19], exec
	v_max_f32_e32 v67, v67, v68

.LBB3_8:
	s_cmp_eq_u32 s90, 0
	s_cbranch_scc1 .Lrec2_p_lo
	s_setprio 1

.LBB3_36:
	s_setprio 0
	s_waitcnt vmcnt(0)
	ds_read_u16 v62, v233
	s_waitcnt lgkmcnt(1)
	v_bfe_u32 v76, v231, 23, 8
	s_cmp_eq_u32 s34, 1
	v_max_u32_e32 v76, 11, v76
	s_cselect_b64 s[24:25], -1, 0
	v_lshlrev_b32_e32 v240, 23, v76
	v_cndmask_b32_e64 v76, 2.0, 1.0, s[24:25]
	s_lshl_b32 s8, s34, 16
	v_mul_f32_e32 v230, v76, v230
	s_and_b32 s67, s8, 0x10000
	v_mov_b32_e32 v58, 0
	v_mov_b32_e32 v59, 0
	v_mov_b32_e32 v60, 0
	v_mov_b32_e32 v61, 0
	v_sub_u32_e32 v164, 0x84000000, v240
	v_pk_fma_f32 v[182:183], v[230:231], v[182:183], v[212:213] op_sel_hi:[0,1,1] neg_lo:[0,0,1] neg_hi:[0,0,1]
	v_pk_fma_f32 v[184:185], v[230:231], v[184:185], v[210:211] op_sel_hi:[0,1,1] neg_lo:[0,0,1] neg_hi:[0,0,1]
	v_pk_fma_f32 v[186:187], v[230:231], v[186:187], v[208:209] op_sel_hi:[0,1,1] neg_lo:[0,0,1] neg_hi:[0,0,1]
	v_pk_fma_f32 v[188:189], v[230:231], v[188:189], v[206:207] op_sel_hi:[0,1,1] neg_lo:[0,0,1] neg_hi:[0,0,1]
	v_fma_mixlo_f16 v58, v182, v164, 0 op_sel_hi:[0,0,0]
	v_fma_mixlo_f16 v59, v184, v164, 0 op_sel_hi:[0,0,0]
	v_fma_mixlo_f16 v60, v186, v164, 0 op_sel_hi:[0,0,0]
	v_fma_mixlo_f16 v61, v188, v164, 0 op_sel_hi:[0,0,0]
	s_waitcnt lgkmcnt(0)
	v_lshl_add_u32 v62, v62, 4, s67
	v_fma_mixhi_f16 v58, v183, v164, 0 op_sel_hi:[0,0,0]
	v_fma_mixhi_f16 v59, v185, v164, 0 op_sel_hi:[0,0,0]
	v_fma_mixhi_f16 v60, v187, v164, 0 op_sel_hi:[0,0,0]
	v_fma_mixhi_f16 v61, v189, v164, 0 op_sel_hi:[0,0,0]
	ds_write_b128 v62, v[58:61]
	ds_read_u16 v62, v233 offset:1024
	v_mov_b32_e32 v58, 0
	v_mov_b32_e32 v59, 0
	v_mov_b32_e32 v60, 0
	v_mov_b32_e32 v61, 0
	v_pk_fma_f32 v[198:199], v[230:231], v[198:199], v[196:197] op_sel_hi:[0,1,1] neg_lo:[0,0,1] neg_hi:[0,0,1]
	v_pk_fma_f32 v[200:201], v[230:231], v[200:201], v[194:195] op_sel_hi:[0,1,1] neg_lo:[0,0,1] neg_hi:[0,0,1]
	v_pk_fma_f32 v[202:203], v[230:231], v[202:203], v[192:193] op_sel_hi:[0,1,1] neg_lo:[0,0,1] neg_hi:[0,0,1]
	v_pk_fma_f32 v[204:205], v[230:231], v[204:205], v[190:191] op_sel_hi:[0,1,1] neg_lo:[0,0,1] neg_hi:[0,0,1]
	v_fma_mixlo_f16 v58, v198, v164, 0 op_sel_hi:[0,0,0]
	v_fma_mixlo_f16 v59, v200, v164, 0 op_sel_hi:[0,0,0]
	v_fma_mixlo_f16 v60, v202, v164, 0 op_sel_hi:[0,0,0]
	v_fma_mixlo_f16 v61, v204, v164, 0 op_sel_hi:[0,0,0]
	s_waitcnt lgkmcnt(0)
	v_lshl_add_u32 v62, v62, 4, s67
	v_fma_mixhi_f16 v58, v199, v164, 0 op_sel_hi:[0,0,0]
	v_fma_mixhi_f16 v59, v201, v164, 0 op_sel_hi:[0,0,0]
	v_fma_mixhi_f16 v60, v203, v164, 0 op_sel_hi:[0,0,0]
	v_fma_mixhi_f16 v61, v205, v164, 0 op_sel_hi:[0,0,0]
	ds_write_b128 v62, v[58:61]
	ds_read_u16 v62, v233 offset:2048
	v_mov_b32_e32 v58, 0
	v_mov_b32_e32 v59, 0
	v_mov_b32_e32 v60, 0
	v_mov_b32_e32 v61, 0
	v_pk_fma_f32 v[214:215], v[230:231], v[214:215], v[180:181] op_sel_hi:[0,1,1] neg_lo:[0,0,1] neg_hi:[0,0,1]
	v_pk_fma_f32 v[216:217], v[230:231], v[216:217], v[178:179] op_sel_hi:[0,1,1] neg_lo:[0,0,1] neg_hi:[0,0,1]
	v_pk_fma_f32 v[218:219], v[230:231], v[218:219], v[176:177] op_sel_hi:[0,1,1] neg_lo:[0,0,1] neg_hi:[0,0,1]
	v_pk_fma_f32 v[220:221], v[230:231], v[220:221], v[174:175] op_sel_hi:[0,1,1] neg_lo:[0,0,1] neg_hi:[0,0,1]
	v_fma_mixlo_f16 v58, v214, v164, 0 op_sel_hi:[0,0,0]
	v_fma_mixlo_f16 v59, v216, v164, 0 op_sel_hi:[0,0,0]
	v_fma_mixlo_f16 v60, v218, v164, 0 op_sel_hi:[0,0,0]
	v_fma_mixlo_f16 v61, v220, v164, 0 op_sel_hi:[0,0,0]
	s_waitcnt lgkmcnt(0)
	v_lshl_add_u32 v62, v62, 4, s67
	v_fma_mixhi_f16 v58, v215, v164, 0 op_sel_hi:[0,0,0]
	v_fma_mixhi_f16 v59, v217, v164, 0 op_sel_hi:[0,0,0]
	v_fma_mixhi_f16 v60, v219, v164, 0 op_sel_hi:[0,0,0]
	v_fma_mixhi_f16 v61, v221, v164, 0 op_sel_hi:[0,0,0]
	ds_write_b128 v62, v[58:61]
	ds_read_u16 v62, v233 offset:3072
	v_mov_b32_e32 v58, 0
	v_mov_b32_e32 v59, 0
	v_mov_b32_e32 v60, 0
	v_mov_b32_e32 v61, 0
	v_pk_fma_f32 v[222:223], v[230:231], v[222:223], v[172:173] op_sel_hi:[0,1,1] neg_lo:[0,0,1] neg_hi:[0,0,1]
	v_pk_fma_f32 v[224:225], v[230:231], v[224:225], v[170:171] op_sel_hi:[0,1,1] neg_lo:[0,0,1] neg_hi:[0,0,1]
	v_pk_fma_f32 v[226:227], v[230:231], v[226:227], v[168:169] op_sel_hi:[0,1,1] neg_lo:[0,0,1] neg_hi:[0,0,1]
	v_pk_fma_f32 v[228:229], v[230:231], v[228:229], v[166:167] op_sel_hi:[0,1,1] neg_lo:[0,0,1] neg_hi:[0,0,1]
	v_fma_mixlo_f16 v58, v222, v164, 0 op_sel_hi:[0,0,0]
	v_fma_mixlo_f16 v59, v224, v164, 0 op_sel_hi:[0,0,0]
	v_fma_mixlo_f16 v60, v226, v164, 0 op_sel_hi:[0,0,0]
	v_fma_mixlo_f16 v61, v228, v164, 0 op_sel_hi:[0,0,0]
	s_waitcnt lgkmcnt(0)
	v_lshl_add_u32 v62, v62, 4, s67
	v_fma_mixhi_f16 v58, v223, v164, 0 op_sel_hi:[0,0,0]
	v_fma_mixhi_f16 v59, v225, v164, 0 op_sel_hi:[0,0,0]
	v_fma_mixhi_f16 v60, v227, v164, 0 op_sel_hi:[0,0,0]
	v_fma_mixhi_f16 v61, v229, v164, 0 op_sel_hi:[0,0,0]
	v_pk_mul_f32 v[206:207], v[38:39], v[74:75]
	v_pk_mul_f32 v[208:209], v[40:41], v[74:75]
	v_pk_mul_f32 v[210:211], v[34:35], v[74:75]
	v_pk_mul_f32 v[212:213], v[36:37], v[74:75]
	v_pk_mul_f32 v[190:191], v[46:47], v[74:75]
	v_pk_mul_f32 v[192:193], v[48:49], v[74:75]
	v_pk_mul_f32 v[194:195], v[42:43], v[74:75]
	v_pk_mul_f32 v[196:197], v[44:45], v[74:75]
	v_pk_mul_f32 v[174:175], v[54:55], v[74:75]
	v_pk_mul_f32 v[176:177], v[56:57], v[74:75]
	v_pk_mul_f32 v[178:179], v[50:51], v[74:75]
	v_pk_mul_f32 v[180:181], v[52:53], v[74:75]
	v_pk_mul_f32 v[166:167], v[124:125], v[74:75]
	v_pk_mul_f32 v[168:169], v[128:129], v[74:75]
	v_pk_mul_f32 v[170:171], v[126:127], v[74:75]
	v_pk_mul_f32 v[172:173], v[130:131], v[74:75]
	s_andn2_b64 vcc, exec, s[12:13]
	s_mov_b64 s[24:25], -1
	ds_write_b128 v62, v[58:61]
	global_load_dwordx4 v[58:61], v[114:115], off
	global_load_dwordx4 v[62:65], v[116:117], off
	global_load_dwordx4 v[66:69], v[118:119], off
	global_load_dwordx4 v[70:73], v[120:121], off
	s_cbranch_vccnz .LBB3_38
	s_mov_b64 s[24:25], 0
